# speedup vs baseline: 1.0159x; 1.0087x over previous
_Z13reduce_kernelPKDF16_Pf:
	s_load_dwordx4 s[4:7], s[0:1], 0x0
	v_lshl_or_b32 v2, s2, 8, v0
	v_lshlrev_b32_e32 v1, 3, v2
	v_mov_b32_e32 v6, 0
	v_mov_b32_e32 v7, 0
	v_mov_b32_e32 v8, 0
	v_mov_b32_e32 v9, 0
	v_add_u32_e32 v81, 0x40000, v1
	v_add_u32_e32 v82, 0x80000, v1
	v_add_u32_e32 v83, 0xc0000, v1
	v_add_u32_e32 v84, 0x100000, v1
	v_add_u32_e32 v85, 0x140000, v1
	v_add_u32_e32 v86, 0x180000, v1
	v_add_u32_e32 v87, 0x1c0000, v1
	v_add_u32_e32 v88, 0x200000, v1
	v_add_u32_e32 v89, 0x240000, v1
	v_add_u32_e32 v90, 0x280000, v1
	v_add_u32_e32 v91, 0x2c0000, v1
	v_add_u32_e32 v92, 0x300000, v1
	v_add_u32_e32 v93, 0x340000, v1
	v_add_u32_e32 v94, 0x380000, v1
	v_add_u32_e32 v95, 0x3c0000, v1
	v_add_u32_e32 v96, 0x400000, v1
	v_add_u32_e32 v97, 0x440000, v1
	v_add_u32_e32 v98, 0x480000, v1
	v_add_u32_e32 v99, 0x4c0000, v1
	v_add_u32_e32 v100, 0x500000, v1
	v_add_u32_e32 v101, 0x540000, v1
	v_add_u32_e32 v102, 0x580000, v1
	v_add_u32_e32 v103, 0x5c0000, v1
	v_add_u32_e32 v104, 0x600000, v1
	v_add_u32_e32 v105, 0x640000, v1
	v_add_u32_e32 v106, 0x680000, v1
	v_add_u32_e32 v107, 0x6c0000, v1
	v_add_u32_e32 v108, 0x700000, v1
	v_add_u32_e32 v109, 0x740000, v1
	v_add_u32_e32 v110, 0x780000, v1
	v_add_u32_e32 v111, 0x7c0000, v1
	s_waitcnt lgkmcnt(0)
	global_load_dwordx2 v[10:11], v1, s[4:5] nt
	global_load_dwordx2 v[12:13], v81, s[4:5] nt
	global_load_dwordx2 v[14:15], v82, s[4:5] nt
	global_load_dwordx2 v[16:17], v83, s[4:5] nt
	global_load_dwordx2 v[18:19], v84, s[4:5] nt
	global_load_dwordx2 v[20:21], v85, s[4:5] nt
	global_load_dwordx2 v[22:23], v86, s[4:5] nt
	global_load_dwordx2 v[24:25], v87, s[4:5] nt
	global_load_dwordx2 v[26:27], v88, s[4:5] nt
	global_load_dwordx2 v[28:29], v89, s[4:5] nt
	global_load_dwordx2 v[30:31], v90, s[4:5] nt
	global_load_dwordx2 v[32:33], v91, s[4:5] nt
	global_load_dwordx2 v[34:35], v92, s[4:5] nt
	global_load_dwordx2 v[36:37], v93, s[4:5] nt
	global_load_dwordx2 v[38:39], v94, s[4:5] nt
	global_load_dwordx2 v[40:41], v95, s[4:5] nt
	global_load_dwordx2 v[42:43], v96, s[4:5] nt
	global_load_dwordx2 v[44:45], v97, s[4:5] nt
	global_load_dwordx2 v[46:47], v98, s[4:5] nt
	global_load_dwordx2 v[48:49], v99, s[4:5] nt
	global_load_dwordx2 v[50:51], v100, s[4:5] nt
	global_load_dwordx2 v[52:53], v101, s[4:5] nt
	global_load_dwordx2 v[54:55], v102, s[4:5] nt
	global_load_dwordx2 v[56:57], v103, s[4:5] nt
	global_load_dwordx2 v[58:59], v104, s[4:5] nt
	global_load_dwordx2 v[60:61], v105, s[4:5] nt
	global_load_dwordx2 v[62:63], v106, s[4:5] nt
	global_load_dwordx2 v[64:65], v107, s[4:5] nt
	global_load_dwordx2 v[66:67], v108, s[4:5] nt
	global_load_dwordx2 v[68:69], v109, s[4:5] nt
	global_load_dwordx2 v[70:71], v110, s[4:5] nt
	global_load_dwordx2 v[72:73], v111, s[4:5] nt
	v_lshlrev_b32_e32 v0, 2, v0
	v_ashrrev_i32_e32 v1, 4, v2
	v_and_b32_e32 v0, 28, v0
	s_movk_i32 s0, 0xffe0
	v_and_or_b32 v0, v1, s0, v0
	v_ashrrev_i32_e32 v1, 31, v0
	v_lshlrev_b64 v[0:1], 8, v[0:1]
	v_lshrrev_b32_e32 v2, 1, v2
	v_lshl_add_u64 v[0:1], s[6:7], 0, v[0:1]
	v_and_b32_e32 v2, 0xfc, v2
	v_mov_b32_e32 v3, 0
	v_lshl_add_u64 v[0:1], v[0:1], 0, v[2:3]
	s_waitcnt vmcnt(31)
	v_cvt_f32_f16_e32 v74, v10
	v_cvt_f32_f16_sdwa v75, v10 dst_sel:DWORD dst_unused:UNUSED_PAD src0_sel:WORD_1
	v_cvt_f32_f16_e32 v76, v11
	v_cvt_f32_f16_sdwa v77, v11 dst_sel:DWORD dst_unused:UNUSED_PAD src0_sel:WORD_1
	v_pk_add_f32 v[6:7], v[6:7], v[74:75]
	v_pk_add_f32 v[8:9], v[8:9], v[76:77]
	s_waitcnt vmcnt(30)
	v_cvt_f32_f16_e32 v74, v12
	v_cvt_f32_f16_sdwa v75, v12 dst_sel:DWORD dst_unused:UNUSED_PAD src0_sel:WORD_1
	v_cvt_f32_f16_e32 v76, v13
	v_cvt_f32_f16_sdwa v77, v13 dst_sel:DWORD dst_unused:UNUSED_PAD src0_sel:WORD_1
	v_pk_add_f32 v[6:7], v[6:7], v[74:75]
	v_pk_add_f32 v[8:9], v[8:9], v[76:77]
	s_waitcnt vmcnt(29)
	v_cvt_f32_f16_e32 v74, v14
	v_cvt_f32_f16_sdwa v75, v14 dst_sel:DWORD dst_unused:UNUSED_PAD src0_sel:WORD_1
	v_cvt_f32_f16_e32 v76, v15
	v_cvt_f32_f16_sdwa v77, v15 dst_sel:DWORD dst_unused:UNUSED_PAD src0_sel:WORD_1
	v_pk_add_f32 v[6:7], v[6:7], v[74:75]
	v_pk_add_f32 v[8:9], v[8:9], v[76:77]
	s_waitcnt vmcnt(28)
	v_cvt_f32_f16_e32 v74, v16
	v_cvt_f32_f16_sdwa v75, v16 dst_sel:DWORD dst_unused:UNUSED_PAD src0_sel:WORD_1
	v_cvt_f32_f16_e32 v76, v17
	v_cvt_f32_f16_sdwa v77, v17 dst_sel:DWORD dst_unused:UNUSED_PAD src0_sel:WORD_1
	v_pk_add_f32 v[6:7], v[6:7], v[74:75]
	v_pk_add_f32 v[8:9], v[8:9], v[76:77]
	s_waitcnt vmcnt(27)
	v_cvt_f32_f16_e32 v74, v18
	v_cvt_f32_f16_sdwa v75, v18 dst_sel:DWORD dst_unused:UNUSED_PAD src0_sel:WORD_1
	v_cvt_f32_f16_e32 v76, v19
	v_cvt_f32_f16_sdwa v77, v19 dst_sel:DWORD dst_unused:UNUSED_PAD src0_sel:WORD_1
	v_pk_add_f32 v[6:7], v[6:7], v[74:75]
	v_pk_add_f32 v[8:9], v[8:9], v[76:77]
	s_waitcnt vmcnt(26)
	v_cvt_f32_f16_e32 v74, v20
	v_cvt_f32_f16_sdwa v75, v20 dst_sel:DWORD dst_unused:UNUSED_PAD src0_sel:WORD_1
	v_cvt_f32_f16_e32 v76, v21
	v_cvt_f32_f16_sdwa v77, v21 dst_sel:DWORD dst_unused:UNUSED_PAD src0_sel:WORD_1
	v_pk_add_f32 v[6:7], v[6:7], v[74:75]
	v_pk_add_f32 v[8:9], v[8:9], v[76:77]
	s_waitcnt vmcnt(25)
	v_cvt_f32_f16_e32 v74, v22
	v_cvt_f32_f16_sdwa v75, v22 dst_sel:DWORD dst_unused:UNUSED_PAD src0_sel:WORD_1
	v_cvt_f32_f16_e32 v76, v23
	v_cvt_f32_f16_sdwa v77, v23 dst_sel:DWORD dst_unused:UNUSED_PAD src0_sel:WORD_1
	v_pk_add_f32 v[6:7], v[6:7], v[74:75]
	v_pk_add_f32 v[8:9], v[8:9], v[76:77]
	s_waitcnt vmcnt(24)
	v_cvt_f32_f16_e32 v74, v24
	v_cvt_f32_f16_sdwa v75, v24 dst_sel:DWORD dst_unused:UNUSED_PAD src0_sel:WORD_1
	v_cvt_f32_f16_e32 v76, v25
	v_cvt_f32_f16_sdwa v77, v25 dst_sel:DWORD dst_unused:UNUSED_PAD src0_sel:WORD_1
	v_pk_add_f32 v[6:7], v[6:7], v[74:75]
	v_pk_add_f32 v[8:9], v[8:9], v[76:77]
	s_waitcnt vmcnt(23)
	v_cvt_f32_f16_e32 v74, v26
	v_cvt_f32_f16_sdwa v75, v26 dst_sel:DWORD dst_unused:UNUSED_PAD src0_sel:WORD_1
	v_cvt_f32_f16_e32 v76, v27
	v_cvt_f32_f16_sdwa v77, v27 dst_sel:DWORD dst_unused:UNUSED_PAD src0_sel:WORD_1
	v_pk_add_f32 v[6:7], v[6:7], v[74:75]
	v_pk_add_f32 v[8:9], v[8:9], v[76:77]
	s_waitcnt vmcnt(22)
	v_cvt_f32_f16_e32 v74, v28
	v_cvt_f32_f16_sdwa v75, v28 dst_sel:DWORD dst_unused:UNUSED_PAD src0_sel:WORD_1
	v_cvt_f32_f16_e32 v76, v29
	v_cvt_f32_f16_sdwa v77, v29 dst_sel:DWORD dst_unused:UNUSED_PAD src0_sel:WORD_1
	v_pk_add_f32 v[6:7], v[6:7], v[74:75]
	v_pk_add_f32 v[8:9], v[8:9], v[76:77]
	s_waitcnt vmcnt(21)
	v_cvt_f32_f16_e32 v74, v30
	v_cvt_f32_f16_sdwa v75, v30 dst_sel:DWORD dst_unused:UNUSED_PAD src0_sel:WORD_1
	v_cvt_f32_f16_e32 v76, v31
	v_cvt_f32_f16_sdwa v77, v31 dst_sel:DWORD dst_unused:UNUSED_PAD src0_sel:WORD_1
	v_pk_add_f32 v[6:7], v[6:7], v[74:75]
	v_pk_add_f32 v[8:9], v[8:9], v[76:77]
	s_waitcnt vmcnt(20)
	v_cvt_f32_f16_e32 v74, v32
	v_cvt_f32_f16_sdwa v75, v32 dst_sel:DWORD dst_unused:UNUSED_PAD src0_sel:WORD_1
	v_cvt_f32_f16_e32 v76, v33
	v_cvt_f32_f16_sdwa v77, v33 dst_sel:DWORD dst_unused:UNUSED_PAD src0_sel:WORD_1
	v_pk_add_f32 v[6:7], v[6:7], v[74:75]
	v_pk_add_f32 v[8:9], v[8:9], v[76:77]
	s_waitcnt vmcnt(19)
	v_cvt_f32_f16_e32 v74, v34
	v_cvt_f32_f16_sdwa v75, v34 dst_sel:DWORD dst_unused:UNUSED_PAD src0_sel:WORD_1
	v_cvt_f32_f16_e32 v76, v35
	v_cvt_f32_f16_sdwa v77, v35 dst_sel:DWORD dst_unused:UNUSED_PAD src0_sel:WORD_1
	v_pk_add_f32 v[6:7], v[6:7], v[74:75]
	v_pk_add_f32 v[8:9], v[8:9], v[76:77]
	s_waitcnt vmcnt(18)
	v_cvt_f32_f16_e32 v74, v36
	v_cvt_f32_f16_sdwa v75, v36 dst_sel:DWORD dst_unused:UNUSED_PAD src0_sel:WORD_1
	v_cvt_f32_f16_e32 v76, v37
	v_cvt_f32_f16_sdwa v77, v37 dst_sel:DWORD dst_unused:UNUSED_PAD src0_sel:WORD_1
	v_pk_add_f32 v[6:7], v[6:7], v[74:75]
	v_pk_add_f32 v[8:9], v[8:9], v[76:77]
	s_waitcnt vmcnt(17)
	v_cvt_f32_f16_e32 v74, v38
	v_cvt_f32_f16_sdwa v75, v38 dst_sel:DWORD dst_unused:UNUSED_PAD src0_sel:WORD_1
	v_cvt_f32_f16_e32 v76, v39
	v_cvt_f32_f16_sdwa v77, v39 dst_sel:DWORD dst_unused:UNUSED_PAD src0_sel:WORD_1
	v_pk_add_f32 v[6:7], v[6:7], v[74:75]
	v_pk_add_f32 v[8:9], v[8:9], v[76:77]
	s_waitcnt vmcnt(16)
	v_cvt_f32_f16_e32 v74, v40
	v_cvt_f32_f16_sdwa v75, v40 dst_sel:DWORD dst_unused:UNUSED_PAD src0_sel:WORD_1
	v_cvt_f32_f16_e32 v76, v41
	v_cvt_f32_f16_sdwa v77, v41 dst_sel:DWORD dst_unused:UNUSED_PAD src0_sel:WORD_1
	v_pk_add_f32 v[6:7], v[6:7], v[74:75]
	v_pk_add_f32 v[8:9], v[8:9], v[76:77]
	s_waitcnt vmcnt(15)
	v_cvt_f32_f16_e32 v74, v42
	v_cvt_f32_f16_sdwa v75, v42 dst_sel:DWORD dst_unused:UNUSED_PAD src0_sel:WORD_1
	v_cvt_f32_f16_e32 v76, v43
	v_cvt_f32_f16_sdwa v77, v43 dst_sel:DWORD dst_unused:UNUSED_PAD src0_sel:WORD_1
	v_pk_add_f32 v[6:7], v[6:7], v[74:75]
	v_pk_add_f32 v[8:9], v[8:9], v[76:77]
	s_waitcnt vmcnt(14)
	v_cvt_f32_f16_e32 v74, v44
	v_cvt_f32_f16_sdwa v75, v44 dst_sel:DWORD dst_unused:UNUSED_PAD src0_sel:WORD_1
	v_cvt_f32_f16_e32 v76, v45
	v_cvt_f32_f16_sdwa v77, v45 dst_sel:DWORD dst_unused:UNUSED_PAD src0_sel:WORD_1
	v_pk_add_f32 v[6:7], v[6:7], v[74:75]
	v_pk_add_f32 v[8:9], v[8:9], v[76:77]
	s_waitcnt vmcnt(13)
	v_cvt_f32_f16_e32 v74, v46
	v_cvt_f32_f16_sdwa v75, v46 dst_sel:DWORD dst_unused:UNUSED_PAD src0_sel:WORD_1
	v_cvt_f32_f16_e32 v76, v47
	v_cvt_f32_f16_sdwa v77, v47 dst_sel:DWORD dst_unused:UNUSED_PAD src0_sel:WORD_1
	v_pk_add_f32 v[6:7], v[6:7], v[74:75]
	v_pk_add_f32 v[8:9], v[8:9], v[76:77]
	s_waitcnt vmcnt(12)
	v_cvt_f32_f16_e32 v74, v48
	v_cvt_f32_f16_sdwa v75, v48 dst_sel:DWORD dst_unused:UNUSED_PAD src0_sel:WORD_1
	v_cvt_f32_f16_e32 v76, v49
	v_cvt_f32_f16_sdwa v77, v49 dst_sel:DWORD dst_unused:UNUSED_PAD src0_sel:WORD_1
	v_pk_add_f32 v[6:7], v[6:7], v[74:75]
	v_pk_add_f32 v[8:9], v[8:9], v[76:77]
	s_waitcnt vmcnt(11)
	v_cvt_f32_f16_e32 v74, v50
	v_cvt_f32_f16_sdwa v75, v50 dst_sel:DWORD dst_unused:UNUSED_PAD src0_sel:WORD_1
	v_cvt_f32_f16_e32 v76, v51
	v_cvt_f32_f16_sdwa v77, v51 dst_sel:DWORD dst_unused:UNUSED_PAD src0_sel:WORD_1
	v_pk_add_f32 v[6:7], v[6:7], v[74:75]
	v_pk_add_f32 v[8:9], v[8:9], v[76:77]
	s_waitcnt vmcnt(10)
	v_cvt_f32_f16_e32 v74, v52
	v_cvt_f32_f16_sdwa v75, v52 dst_sel:DWORD dst_unused:UNUSED_PAD src0_sel:WORD_1
	v_cvt_f32_f16_e32 v76, v53
	v_cvt_f32_f16_sdwa v77, v53 dst_sel:DWORD dst_unused:UNUSED_PAD src0_sel:WORD_1
	v_pk_add_f32 v[6:7], v[6:7], v[74:75]
	v_pk_add_f32 v[8:9], v[8:9], v[76:77]
	s_waitcnt vmcnt(9)
	v_cvt_f32_f16_e32 v74, v54
	v_cvt_f32_f16_sdwa v75, v54 dst_sel:DWORD dst_unused:UNUSED_PAD src0_sel:WORD_1
	v_cvt_f32_f16_e32 v76, v55
	v_cvt_f32_f16_sdwa v77, v55 dst_sel:DWORD dst_unused:UNUSED_PAD src0_sel:WORD_1
	v_pk_add_f32 v[6:7], v[6:7], v[74:75]
	v_pk_add_f32 v[8:9], v[8:9], v[76:77]
	s_waitcnt vmcnt(8)
	v_cvt_f32_f16_e32 v74, v56
	v_cvt_f32_f16_sdwa v75, v56 dst_sel:DWORD dst_unused:UNUSED_PAD src0_sel:WORD_1
	v_cvt_f32_f16_e32 v76, v57
	v_cvt_f32_f16_sdwa v77, v57 dst_sel:DWORD dst_unused:UNUSED_PAD src0_sel:WORD_1
	v_pk_add_f32 v[6:7], v[6:7], v[74:75]
	v_pk_add_f32 v[8:9], v[8:9], v[76:77]
	s_waitcnt vmcnt(7)
	v_cvt_f32_f16_e32 v74, v58
	v_cvt_f32_f16_sdwa v75, v58 dst_sel:DWORD dst_unused:UNUSED_PAD src0_sel:WORD_1
	v_cvt_f32_f16_e32 v76, v59
	v_cvt_f32_f16_sdwa v77, v59 dst_sel:DWORD dst_unused:UNUSED_PAD src0_sel:WORD_1
	v_pk_add_f32 v[6:7], v[6:7], v[74:75]
	v_pk_add_f32 v[8:9], v[8:9], v[76:77]
	s_waitcnt vmcnt(6)
	v_cvt_f32_f16_e32 v74, v60
	v_cvt_f32_f16_sdwa v75, v60 dst_sel:DWORD dst_unused:UNUSED_PAD src0_sel:WORD_1
	v_cvt_f32_f16_e32 v76, v61
	v_cvt_f32_f16_sdwa v77, v61 dst_sel:DWORD dst_unused:UNUSED_PAD src0_sel:WORD_1
	v_pk_add_f32 v[6:7], v[6:7], v[74:75]
	v_pk_add_f32 v[8:9], v[8:9], v[76:77]
	s_waitcnt vmcnt(5)
	v_cvt_f32_f16_e32 v74, v62
	v_cvt_f32_f16_sdwa v75, v62 dst_sel:DWORD dst_unused:UNUSED_PAD src0_sel:WORD_1
	v_cvt_f32_f16_e32 v76, v63
	v_cvt_f32_f16_sdwa v77, v63 dst_sel:DWORD dst_unused:UNUSED_PAD src0_sel:WORD_1
	v_pk_add_f32 v[6:7], v[6:7], v[74:75]
	v_pk_add_f32 v[8:9], v[8:9], v[76:77]
	s_waitcnt vmcnt(4)
	v_cvt_f32_f16_e32 v74, v64
	v_cvt_f32_f16_sdwa v75, v64 dst_sel:DWORD dst_unused:UNUSED_PAD src0_sel:WORD_1
	v_cvt_f32_f16_e32 v76, v65
	v_cvt_f32_f16_sdwa v77, v65 dst_sel:DWORD dst_unused:UNUSED_PAD src0_sel:WORD_1
	v_pk_add_f32 v[6:7], v[6:7], v[74:75]
	v_pk_add_f32 v[8:9], v[8:9], v[76:77]
	s_waitcnt vmcnt(3)
	v_cvt_f32_f16_e32 v74, v66
	v_cvt_f32_f16_sdwa v75, v66 dst_sel:DWORD dst_unused:UNUSED_PAD src0_sel:WORD_1
	v_cvt_f32_f16_e32 v76, v67
	v_cvt_f32_f16_sdwa v77, v67 dst_sel:DWORD dst_unused:UNUSED_PAD src0_sel:WORD_1
	v_pk_add_f32 v[6:7], v[6:7], v[74:75]
	v_pk_add_f32 v[8:9], v[8:9], v[76:77]
	s_waitcnt vmcnt(2)
	v_cvt_f32_f16_e32 v74, v68
	v_cvt_f32_f16_sdwa v75, v68 dst_sel:DWORD dst_unused:UNUSED_PAD src0_sel:WORD_1
	v_cvt_f32_f16_e32 v76, v69
	v_cvt_f32_f16_sdwa v77, v69 dst_sel:DWORD dst_unused:UNUSED_PAD src0_sel:WORD_1
	v_pk_add_f32 v[6:7], v[6:7], v[74:75]
	v_pk_add_f32 v[8:9], v[8:9], v[76:77]
	s_waitcnt vmcnt(1)
	v_cvt_f32_f16_e32 v74, v70
	v_cvt_f32_f16_sdwa v75, v70 dst_sel:DWORD dst_unused:UNUSED_PAD src0_sel:WORD_1
	v_cvt_f32_f16_e32 v76, v71
	v_cvt_f32_f16_sdwa v77, v71 dst_sel:DWORD dst_unused:UNUSED_PAD src0_sel:WORD_1
	v_pk_add_f32 v[6:7], v[6:7], v[74:75]
	v_pk_add_f32 v[8:9], v[8:9], v[76:77]
	s_waitcnt vmcnt(0)
	v_cvt_f32_f16_e32 v74, v72
	v_cvt_f32_f16_sdwa v75, v72 dst_sel:DWORD dst_unused:UNUSED_PAD src0_sel:WORD_1
	v_cvt_f32_f16_e32 v76, v73
	v_cvt_f32_f16_sdwa v77, v73 dst_sel:DWORD dst_unused:UNUSED_PAD src0_sel:WORD_1
	v_pk_add_f32 v[6:7], v[6:7], v[74:75]
	v_pk_add_f32 v[8:9], v[8:9], v[76:77]
	v_mul_f32_e32 v2, 0x3b800000, v6
	global_store_dword v[0:1], v2, off
	v_mul_f32_e32 v2, 0x3b800000, v7
	global_store_dword v[0:1], v2, off offset:256
	v_mul_f32_e32 v2, 0x3b800000, v8
	global_store_dword v[0:1], v2, off offset:512
	v_mul_f32_e32 v2, 0x3b800000, v9
	global_store_dword v[0:1], v2, off offset:768
	s_endpgm
